# router: the expert bias add also deferred to the batched tail (per-lane LDS gather by group) -- no LDS round trip per row
# baseline (speedup 1.0000x reference)
; __device__ __forceinline__ void router_ph(const int WID_, const bf16* __restrict__ x3, const float* __restrict__ nw, const float* __restrict__ wrg, const float* __restrict__ brg, ...
;     ...
;     for (int m = tile * 256 + wv; m < tile * 256 + 256; m += 8) {
;         float h[16]; float s = 0.f;
; #pragma unroll
;         for (int j = 0; j < 2; ++j) { const unsigned wd[4] = {nx[j].x, nx[j].y, nx[j].z, nx[j].w};
; #pragma unroll
;             for (int q = 0; q < 4; ++q) { const float lo = __builtin_bit_cast(float, wd[q] << 16), hi = __builtin_bit_cast(float, wd[q] & 0xffff0000u); h[8 * j + 2 * q] = lo; h[8 * j + 2 * q + 1] = hi; s += lo * lo + hi * hi; } }
;         { const int mn = min(m + 8, tile * 256 + 248 + wv); const uint4* xr = (const uint4*)(x3 + (size_t)mn * D);
; #pragma unroll
;           for (int j = 0; j < 2; ++j) nx[j] = xr[lane + 64 * j]; }
;         s = wave_sum(s);
;         const float rs = rsqrtf(s * (1.f / D) + 1e-6f);
;         float l1[4] = {0.f, 0.f, 0.f, 0.f};
; #pragma unroll
;         for (int j = 0; j < 2; ++j) {
;             const int k0 = (lane + 64 * j) * 8;
;             const float4 ga = gw[2 * j], gb = gw[2 * j + 1];
;             h[8 * j] *= rs * ga.x; h[8 * j + 1] *= rs * ga.y; h[8 * j + 2] *= rs * ga.z; h[8 * j + 3] *= rs * ga.w;
;             h[8 * j + 4] *= rs * gb.x; h[8 * j + 5] *= rs * gb.y; h[8 * j + 6] *= rs * gb.z; h[8 * j + 7] *= rs * gb.w;
; #pragma unroll
;             for (int e = 0; e < 8; ++e) { const h4 w = *(const h4*)(wg16 + (k0 + e) * 4); const float x = h[8 * j + e];
;                 l1[0] += x * (float)w[0]; l1[1] += x * (float)w[1]; l1[2] += x * (float)w[2]; l1[3] += x * (float)w[3]; }
.LBB0_2145:
	v_and_b32_e32 v90, 0xffff0000, v16
	v_and_b32_e32 v92, 0xffff0000, v17
	v_lshlrev_b32_e32 v59, 16, v16
	v_mul_f32_e32 v14, v90, v90
	v_lshlrev_b32_e32 v91, 16, v17
	v_mul_f32_e32 v16, v92, v92
	v_fmac_f32_e32 v14, v59, v59
	v_fmac_f32_e32 v16, v91, v91
	v_and_b32_e32 v94, 0xffff0000, v18
	v_add_f32_e32 v14, v16, v14
	v_lshlrev_b32_e32 v93, 16, v18
	v_mul_f32_e32 v16, v94, v94
	v_fmac_f32_e32 v16, v93, v93
	v_and_b32_e32 v96, 0xffff0000, v19
	v_add_f32_e32 v14, v16, v14
	v_lshlrev_b32_e32 v95, 16, v19
	v_mul_f32_e32 v16, v96, v96
	v_and_b32_e32 v85, 0xffff0000, v13
	v_and_b32_e32 v84, 0xffff0000, v12
	v_fmac_f32_e32 v16, v95, v95
	v_lshlrev_b32_e32 v27, 16, v13
	v_lshlrev_b32_e32 v26, 16, v12
	v_pk_mul_f32 v[12:13], v[84:85], v[84:85]
	v_add_f32_e32 v14, v16, v14
	v_pk_fma_f32 v[16:17], v[26:27], v[26:27], v[12:13]
	v_and_b32_e32 v86, 0xffff0000, v2
	v_add_f32_e32 v14, v16, v14
	v_add_f32_e32 v88, v17, v14
	v_and_b32_e32 v14, 0xffff0000, v15
	v_lshlrev_b32_e32 v15, 16, v15
	v_lshlrev_b32_e32 v87, 16, v2
	v_mov_b32_e32 v82, v14
	v_mov_b32_e32 v83, v86
	v_mov_b32_e32 v80, v15
	v_mov_b32_e32 v81, v87
	v_pk_mul_f32 v[82:83], v[82:83], v[82:83]
	s_add_i32 s4, s44, 16
	v_pk_fma_f32 v[80:81], v[80:81], v[80:81], v[82:83]
	s_min_i32 s4, s4, s33
	v_add_f32_e32 v2, v81, v88
	v_add_f32_e32 v2, v80, v2
	v_mov_b32_e32 v80, 0
	s_ashr_i32 s5, s4, 31
	v_add_f32_dpp v2, v2, v2 quad_perm:[1,0,3,2] row_mask:0xf bank_mask:0xf bound_ctrl:1
	s_lshl_b64 s[4:5], s[4:5], 11
	v_lshl_add_u64 v[12:13], v[10:11], 0, s[4:5]
	v_add_f32_dpp v2, v2, v2 quad_perm:[2,3,0,1] row_mask:0xf bank_mask:0xf bound_ctrl:1
	ds_read_b128 v[16:19], v21 offset:256
	ds_read_b128 v[22:25], v52 offset:256
	ds_read_b128 v[60:63], v53 offset:256
	ds_read_b128 v[64:67], v54 offset:256
	ds_read_b128 v[68:71], v55 offset:256
	ds_read_b128 v[72:75], v56 offset:256
	ds_read_b128 v[76:79], v57 offset:256
	v_add_f32_dpp v2, v2, v2 row_half_mirror row_mask:0xf bank_mask:0xf bound_ctrl:1
	s_add_i32 s5, 0, 0x12100
	s_waitcnt lgkmcnt(0)
	v_cvt_f32_f16_sdwa v89, v77 dst_sel:DWORD dst_unused:UNUSED_PAD src0_sel:WORD_1
	v_add_f32_dpp v2, v2, v2 row_mirror row_mask:0xf bank_mask:0xf bound_ctrl:1
	v_cvt_f32_f16_sdwa v88, v79 dst_sel:DWORD dst_unused:UNUSED_PAD src0_sel:WORD_1
	s_nop 0
	v_mov_b32_dpp v80, v2 row_bcast:15 row_mask:0xa bank_mask:0xf
	v_add_f32_e32 v2, v2, v80
	v_mov_b32_e32 v80, 0
	s_nop 1
	v_mov_b32_dpp v80, v2 row_bcast:31 row_mask:0xc bank_mask:0xf
	v_add_f32_e32 v2, v2, v80
	s_nop 0
	v_readlane_b32 s4, v2, 63
	s_nop 1
	v_fma_f32 v2, s4, v196, v194
	v_mul_f32_e32 v80, 0x4b800000, v2
	v_cmp_gt_f32_e32 vcc, s64, v2
	s_nop 1
	v_cndmask_b32_e32 v2, v2, v80, vcc
	v_rsq_f32_e32 v2, v2
	ds_read_b128 v[80:83], v58 offset:256
	v_mul_f32_e32 v97, 0x45800000, v2
	v_cndmask_b32_e32 v2, v2, v97, vcc
	v_mul_f32_e32 v97, v29, v2
	v_mul_f32_e32 v97, v97, v59
	v_mul_f32_e32 v59, v31, v2
	v_mul_f32_e32 v90, v59, v90
	v_mul_f32_e32 v59, v30, v2
	v_mul_f32_e32 v91, v59, v91
	v_mul_f32_e32 v59, v3, v2
	v_mul_f32_e32 v92, v59, v92
	v_mul_f32_e32 v59, v33, v2
	v_mul_f32_e32 v93, v59, v93
	v_mul_f32_e32 v59, v32, v2
	v_mul_f32_e32 v94, v59, v94
	v_mul_f32_e32 v59, v6, v2
	v_mul_f32_e32 v95, v59, v95
	v_mul_f32_e32 v59, v7, v2
	v_mul_f32_e32 v96, v59, v96
	v_fma_mix_f32 v59, v97, v16, 0 op_sel_hi:[0,1,0]
	v_fma_mix_f32 v16, v97, v16, 0 op_sel:[0,1,0] op_sel_hi:[0,1,0]
	v_fma_mix_f32 v16, v90, v18, v16 op_sel:[0,1,0] op_sel_hi:[0,1,0]
	v_fma_mix_f32 v16, v91, v22, v16 op_sel:[0,1,0] op_sel_hi:[0,1,0]
	v_fma_mix_f32 v16, v92, v24, v16 op_sel:[0,1,0] op_sel_hi:[0,1,0]
	v_fma_mix_f32 v98, v97, v17, 0 op_sel_hi:[0,1,0]
	v_fma_mix_f32 v17, v97, v17, 0 op_sel:[0,1,0] op_sel_hi:[0,1,0]
	v_fma_mix_f32 v16, v93, v60, v16 op_sel:[0,1,0] op_sel_hi:[0,1,0]
	v_fma_mix_f32 v17, v90, v19, v17 op_sel:[0,1,0] op_sel_hi:[0,1,0]
	v_fma_mix_f32 v16, v94, v62, v16 op_sel:[0,1,0] op_sel_hi:[0,1,0]
	v_fma_mix_f32 v59, v90, v18, v59 op_sel_hi:[0,1,0]
	v_fma_mix_f32 v17, v91, v23, v17 op_sel:[0,1,0] op_sel_hi:[0,1,0]
	v_fma_mix_f32 v16, v95, v64, v16 op_sel:[0,1,0] op_sel_hi:[0,1,0]
	v_fma_mix_f32 v18, v90, v19, v98 op_sel_hi:[0,1,0]
	v_fma_mix_f32 v19, v91, v22, v59 op_sel_hi:[0,1,0]
	v_fma_mix_f32 v17, v92, v25, v17 op_sel:[0,1,0] op_sel_hi:[0,1,0]
	v_fma_mix_f32 v22, v96, v66, v16 op_sel:[0,1,0] op_sel_hi:[0,1,0]
	v_mul_f32_e32 v16, v8, v2
	v_fma_mix_f32 v18, v91, v23, v18 op_sel_hi:[0,1,0]
	v_fma_mix_f32 v19, v92, v24, v19 op_sel_hi:[0,1,0]
	v_fma_mix_f32 v17, v93, v61, v17 op_sel:[0,1,0] op_sel_hi:[0,1,0]
	v_mul_f32_e32 v98, v16, v26
	v_mul_f32_e32 v16, v9, v2
	v_fma_mix_f32 v18, v92, v25, v18 op_sel_hi:[0,1,0]
	v_fma_mix_f32 v19, v93, v60, v19 op_sel_hi:[0,1,0]
	v_fma_mix_f32 v17, v94, v63, v17 op_sel:[0,1,0] op_sel_hi:[0,1,0]
	v_mul_f32_e32 v84, v16, v84
	v_mul_f32_e32 v16, v35, v2
	v_fma_mix_f32 v18, v93, v61, v18 op_sel_hi:[0,1,0]
	v_fma_mix_f32 v19, v94, v62, v19 op_sel_hi:[0,1,0]
	v_fma_mix_f32 v17, v95, v65, v17 op_sel:[0,1,0] op_sel_hi:[0,1,0]
	v_mul_f32_e32 v99, v16, v27
	v_mul_f32_e32 v16, v34, v2
	v_fma_mix_f32 v18, v94, v63, v18 op_sel_hi:[0,1,0]
	v_fma_mix_f32 v19, v95, v64, v19 op_sel_hi:[0,1,0]
	v_fma_mix_f32 v23, v96, v67, v17 op_sel:[0,1,0] op_sel_hi:[0,1,0]
	v_mul_f32_e32 v85, v16, v85
	v_pk_mul_f32 v[16:17], v[0:1], v[2:3] op_sel_hi:[1,0]
	v_fma_mix_f32 v18, v95, v65, v18 op_sel_hi:[0,1,0]
	v_fma_mix_f32 v19, v96, v66, v19 op_sel_hi:[0,1,0]
	v_pk_mul_f32 v[26:27], v[16:17], v[86:87]
	v_pk_mul_f32 v[16:17], v[4:5], v[2:3] op_sel_hi:[1,0]
	v_fma_mix_f32 v18, v96, v67, v18 op_sel_hi:[0,1,0]
	v_pk_mul_f32 v[24:25], v[16:17], v[14:15]
	v_fma_mix_f32 v14, v98, v68, v19 op_sel_hi:[0,1,0]
	v_fma_mix_f32 v15, v98, v68, v22 op_sel:[0,1,0] op_sel_hi:[0,1,0]
	v_fma_mix_f32 v16, v98, v69, v18 op_sel_hi:[0,1,0]
	v_fma_mix_f32 v17, v98, v69, v23 op_sel:[0,1,0] op_sel_hi:[0,1,0]
	v_fma_mix_f32 v14, v84, v70, v14 op_sel_hi:[0,1,0]
	v_fma_mix_f32 v15, v84, v70, v15 op_sel:[0,1,0] op_sel_hi:[0,1,0]
	v_fma_mix_f32 v16, v84, v71, v16 op_sel_hi:[0,1,0]
	v_fma_mix_f32 v17, v84, v71, v17 op_sel:[0,1,0] op_sel_hi:[0,1,0]
	v_fma_mix_f32 v14, v99, v72, v14 op_sel_hi:[0,1,0]
	v_fma_mix_f32 v15, v99, v72, v15 op_sel:[0,1,0] op_sel_hi:[0,1,0]
	v_fma_mix_f32 v16, v99, v73, v16 op_sel_hi:[0,1,0]
	v_fma_mix_f32 v17, v99, v73, v17 op_sel:[0,1,0] op_sel_hi:[0,1,0]
	v_fma_mix_f32 v14, v85, v74, v14 op_sel_hi:[0,1,0]
	v_fma_mix_f32 v22, v85, v74, v15 op_sel:[0,1,0] op_sel_hi:[0,1,0]
	v_fma_mix_f32 v23, v85, v75, v16 op_sel_hi:[0,1,0]
	v_fma_mix_f32 v16, v85, v75, v17 op_sel:[0,1,0] op_sel_hi:[0,1,0]
	v_fma_mix_f32 v18, v27, v76, v14 op_sel_hi:[0,1,0]
	v_pk_mul_f32 v[14:15], v[26:27], v[88:89]
	v_cvt_f32_f16_sdwa v17, v76 dst_sel:DWORD dst_unused:UNUSED_PAD src0_sel:WORD_1
	v_add_f32_e32 v15, v15, v16
	v_cvt_f32_f16_sdwa v16, v78 dst_sel:DWORD dst_unused:UNUSED_PAD src0_sel:WORD_1
	v_fma_mix_f32 v59, v26, v78, v18 op_sel_hi:[0,1,0]
	v_cvt_f32_f16_e32 v19, v77
	v_cvt_f32_f16_e32 v18, v79
	v_pk_mul_f32 v[16:17], v[26:27], v[16:17]
	s_waitcnt lgkmcnt(0)
; __device__ __forceinline__ void router_ph(const int WID_, const bf16* __restrict__ x3, const float* __restrict__ nw, const float* __restrict__ wrg, const float* __restrict__ brg, ...
;     ...
;         { const int mn = min(m + 8, tile * 256 + 248 + wv); const uint4* xr = (const uint4*)(x3 + (size_t)mn * D);
; #pragma unroll
;           for (int j = 0; j < 2; ++j) nx[j] = xr[lane + 64 * j]; }
;     ...
;             for (int e = 0; e < 8; ++e) { const h4 w = *(const h4*)(wg16 + (k0 + e) * 4); const float x = h[8 * j + e];
;                 l1[0] += x * (float)w[0]; l1[1] += x * (float)w[1]; l1[2] += x * (float)w[2]; l1[3] += x * (float)w[3]; }
;         }
; #pragma unroll
;         for (int i = 0; i < 4; ++i) l1[i] = wave_sum(l1[i]) + brg_l[i];
;         int grp = 0; float best = l1[0];
; #pragma unroll
;         for (int i = 1; i < 4; ++i) if (l1[i] > best) { best = l1[i]; grp = i; }
;         float se = 0.f;
; #pragma unroll
;         for (int i = 0; i < 4; ++i) se += __expf(l1[i] - best);
;         const float g1 = 1.f / se;
;         float l2[8] = {};
;         const _Float16* we = we16 + (size_t)grp * D * 8;
; #pragma unroll
;         for (int j = 0; j < 2; ++j) {
;             const int k0 = (lane + 64 * j) * 8;
; #pragma unroll
;             for (int e = 0; e < 8; ++e) { const float x = h[8 * j + e]; const h8 w = *(const h8*)(we + (k0 + e) * 8);
; #pragma unroll
;                 for (int q = 0; q < 8; ++q) l2[q] += x * (float)w[q]; }
	v_fma_mix_f32 v59, v25, v80, v59 op_sel_hi:[0,1,0]
	v_add_f32_e32 v17, v17, v22
	v_add_f32_e32 v22, v16, v17
	v_pk_mul_f32 v[16:17], v[26:27], v[18:19]
	v_cvt_f32_f16_sdwa v19, v81 dst_sel:DWORD dst_unused:UNUSED_PAD src0_sel:WORD_1
	v_cvt_f32_f16_sdwa v18, v83 dst_sel:DWORD dst_unused:UNUSED_PAD src0_sel:WORD_1
	v_add_f32_e32 v17, v17, v23
	v_add_f32_e32 v23, v16, v17
	v_add_f32_e32 v16, v14, v15
	v_pk_mul_f32 v[14:15], v[24:25], v[18:19]
	v_cvt_f32_f16_sdwa v17, v80 dst_sel:DWORD dst_unused:UNUSED_PAD src0_sel:WORD_1
	v_add_f32_e32 v15, v15, v16
	v_cvt_f32_f16_sdwa v16, v82 dst_sel:DWORD dst_unused:UNUSED_PAD src0_sel:WORD_1
	v_cvt_f32_f16_e32 v19, v81
	v_cvt_f32_f16_e32 v18, v83
	v_fma_mix_f32 v59, v24, v82, v59 op_sel_hi:[0,1,0]
	v_pk_mul_f32 v[16:17], v[24:25], v[16:17]
	s_nop 0
	v_add_f32_e32 v17, v17, v22
	v_add_f32_e32 v22, v16, v17
	v_pk_mul_f32 v[16:17], v[24:25], v[18:19]
	v_add_f32_e32 v19, v14, v15
	v_add_f32_e32 v17, v17, v23
	v_add_f32_e32 v18, v16, v17
	v_mov_b32_e32 v14, s5
	ds_read_b128 v[100:103], v14
	v_add_f32_dpp v59, v59, v59 quad_perm:[1,0,3,2] row_mask:0xf bank_mask:0xf bound_ctrl:1
	v_add_f32_dpp v22, v22, v22 quad_perm:[1,0,3,2] row_mask:0xf bank_mask:0xf bound_ctrl:1
	v_add_f32_dpp v18, v18, v18 quad_perm:[1,0,3,2] row_mask:0xf bank_mask:0xf bound_ctrl:1
	v_add_f32_dpp v19, v19, v19 quad_perm:[1,0,3,2] row_mask:0xf bank_mask:0xf bound_ctrl:1
	v_add_f32_dpp v59, v59, v59 quad_perm:[2,3,0,1] row_mask:0xf bank_mask:0xf bound_ctrl:1
	v_add_f32_dpp v22, v22, v22 quad_perm:[2,3,0,1] row_mask:0xf bank_mask:0xf bound_ctrl:1
	v_add_f32_dpp v18, v18, v18 quad_perm:[2,3,0,1] row_mask:0xf bank_mask:0xf bound_ctrl:1
	v_add_f32_dpp v19, v19, v19 quad_perm:[2,3,0,1] row_mask:0xf bank_mask:0xf bound_ctrl:1
	v_add_f32_dpp v59, v59, v59 row_half_mirror row_mask:0xf bank_mask:0xf bound_ctrl:1
	v_add_f32_dpp v22, v22, v22 row_half_mirror row_mask:0xf bank_mask:0xf bound_ctrl:1
	v_add_f32_dpp v18, v18, v18 row_half_mirror row_mask:0xf bank_mask:0xf bound_ctrl:1
	v_add_f32_dpp v19, v19, v19 row_half_mirror row_mask:0xf bank_mask:0xf bound_ctrl:1
	v_add_f32_dpp v59, v59, v59 row_mirror row_mask:0xf bank_mask:0xf bound_ctrl:1
	v_add_f32_dpp v22, v22, v22 row_mirror row_mask:0xf bank_mask:0xf bound_ctrl:1
	v_add_f32_dpp v18, v18, v18 row_mirror row_mask:0xf bank_mask:0xf bound_ctrl:1
	v_add_f32_dpp v19, v19, v19 row_mirror row_mask:0xf bank_mask:0xf bound_ctrl:1
	v_mov_b32_e32 v104, 0
	v_mov_b32_e32 v105, 0
	v_mov_b32_e32 v106, 0
	v_mov_b32_e32 v107, 0
	v_mov_b32_dpp v104, v59 row_bcast:15 row_mask:0xa bank_mask:0xf
	v_mov_b32_dpp v105, v22 row_bcast:15 row_mask:0xa bank_mask:0xf
	v_mov_b32_dpp v106, v18 row_bcast:15 row_mask:0xa bank_mask:0xf
	v_mov_b32_dpp v107, v19 row_bcast:15 row_mask:0xa bank_mask:0xf
	v_add_f32_e32 v59, v59, v104
	v_add_f32_e32 v22, v22, v105
	v_add_f32_e32 v18, v18, v106
	v_add_f32_e32 v19, v19, v107
	v_mov_b32_e32 v104, 0
	v_mov_b32_e32 v105, 0
	v_mov_b32_e32 v106, 0
	v_mov_b32_e32 v107, 0
	v_mov_b32_dpp v104, v59 row_bcast:31 row_mask:0xc bank_mask:0xf
	v_mov_b32_dpp v105, v22 row_bcast:31 row_mask:0xc bank_mask:0xf
	v_mov_b32_dpp v106, v18 row_bcast:31 row_mask:0xc bank_mask:0xf
	v_mov_b32_dpp v107, v19 row_bcast:31 row_mask:0xc bank_mask:0xf
	v_add_f32_e32 v59, v59, v104
	v_add_f32_e32 v22, v22, v105
	v_add_f32_e32 v18, v18, v106
	v_add_f32_e32 v19, v19, v107
	v_readlane_b32 s4, v59, 63
	v_readlane_b32 s5, v22, 63
	v_readlane_b32 s6, v18, 63
	v_readlane_b32 s7, v19, 63
	s_waitcnt lgkmcnt(0)
	v_pk_add_f32 v[22:23], s[4:5], v[100:101]
	v_add_f32_e32 v59, s6, v102
	v_add_f32_e32 v60, s7, v103
	v_cmp_gt_f32_e64 s[4:5], v23, v22
	s_nop 1
	v_cndmask_b32_e64 v14, v22, v23, s[4:5]
	v_cmp_gt_f32_e64 s[6:7], v59, v14
	s_nop 1
	v_cndmask_b32_e64 v61, v14, v59, s[6:7]
	v_cndmask_b32_e64 v14, 0, 1, s[4:5]
	s_and_b64 s[4:5], s[6:7], exec
	v_cmp_gt_f32_e32 vcc, v60, v61
	v_readfirstlane_b32 s4, v14
	s_cselect_b32 s6, 2, s4
	s_and_b64 s[4:5], vcc, exec
	s_cselect_b32 s49, 3, s6
	s_lshl_b32 s4, s49, 14
	s_add_i32 s48, s4, 0
	global_load_dwordx4 v[16:19], v[12:13], off
	s_nop 0
	global_load_dwordx4 v[12:15], v[12:13], off offset:1024
	v_add_u32_e32 v112, s48, v36
	ds_read_b128 v[132:135], v112 offset:8448
	ds_read_b128 v[136:139], v112 offset:9472
	ds_read_b128 v[140:143], v112 offset:10496
	ds_read_b128 v[144:147], v112 offset:11520
	ds_read_b128 v[148:151], v112 offset:12544
	ds_read_b128 v[152:155], v112 offset:13568
	ds_read_b128 v[156:159], v112 offset:14592
	ds_read_b128 v[160:163], v112 offset:15616
	ds_read_b128 v[164:167], v112 offset:16640
	ds_read_b128 v[168:171], v112 offset:17664
	ds_read_b128 v[172:175], v112 offset:18688
	ds_read_b128 v[176:179], v112 offset:19712
	s_waitcnt lgkmcnt(11)
	v_fma_mix_f32 v70, v97, v132, 0 op_sel_hi:[0,1,0]
	v_fma_mix_f32 v71, v97, v132, 0 op_sel:[0,1,0] op_sel_hi:[0,1,0]
	v_fma_mix_f32 v72, v97, v133, 0 op_sel_hi:[0,1,0]
	v_fma_mix_f32 v73, v97, v133, 0 op_sel:[0,1,0] op_sel_hi:[0,1,0]
	v_fma_mix_f32 v74, v97, v134, 0 op_sel_hi:[0,1,0]
	v_fma_mix_f32 v75, v97, v134, 0 op_sel:[0,1,0] op_sel_hi:[0,1,0]
	v_fma_mix_f32 v76, v97, v135, 0 op_sel_hi:[0,1,0]
	v_fma_mix_f32 v77, v97, v135, 0 op_sel:[0,1,0] op_sel_hi:[0,1,0]
	s_waitcnt lgkmcnt(10)
	v_fma_mix_f32 v70, v90, v136, v70 op_sel_hi:[0,1,0]
	v_fma_mix_f32 v71, v90, v136, v71 op_sel:[0,1,0] op_sel_hi:[0,1,0]
	v_fma_mix_f32 v72, v90, v137, v72 op_sel_hi:[0,1,0]
	v_fma_mix_f32 v73, v90, v137, v73 op_sel:[0,1,0] op_sel_hi:[0,1,0]
	v_fma_mix_f32 v74, v90, v138, v74 op_sel_hi:[0,1,0]
	v_fma_mix_f32 v75, v90, v138, v75 op_sel:[0,1,0] op_sel_hi:[0,1,0]
	v_fma_mix_f32 v76, v90, v139, v76 op_sel_hi:[0,1,0]
	v_fma_mix_f32 v77, v90, v139, v77 op_sel:[0,1,0] op_sel_hi:[0,1,0]
	s_waitcnt lgkmcnt(9)
; __device__ __forceinline__ void router_ph(const int WID_, const bf16* __restrict__ x3, const float* __restrict__ nw, const float* __restrict__ wrg, const float* __restrict__ brg, ...
;     ...
;         float l2[8] = {};
;         const _Float16* we = we16 + (size_t)grp * D * 8;
; #pragma unroll
;         for (int j = 0; j < 2; ++j) {
;             const int k0 = (lane + 64 * j) * 8;
; #pragma unroll
;             for (int e = 0; e < 8; ++e) { const float x = h[8 * j + e]; const h8 w = *(const h8*)(we + (k0 + e) * 8);
; #pragma unroll
;                 for (int q = 0; q < 8; ++q) l2[q] += x * (float)w[q]; }
;         }
	v_fma_mix_f32 v70, v91, v140, v70 op_sel_hi:[0,1,0]
	v_fma_mix_f32 v71, v91, v140, v71 op_sel:[0,1,0] op_sel_hi:[0,1,0]
	v_fma_mix_f32 v72, v91, v141, v72 op_sel_hi:[0,1,0]
	v_fma_mix_f32 v73, v91, v141, v73 op_sel:[0,1,0] op_sel_hi:[0,1,0]
	v_fma_mix_f32 v74, v91, v142, v74 op_sel_hi:[0,1,0]
	v_fma_mix_f32 v75, v91, v142, v75 op_sel:[0,1,0] op_sel_hi:[0,1,0]
	v_fma_mix_f32 v76, v91, v143, v76 op_sel_hi:[0,1,0]
	v_fma_mix_f32 v77, v91, v143, v77 op_sel:[0,1,0] op_sel_hi:[0,1,0]
	s_waitcnt lgkmcnt(8)
	v_fma_mix_f32 v70, v92, v144, v70 op_sel_hi:[0,1,0]
	v_fma_mix_f32 v71, v92, v144, v71 op_sel:[0,1,0] op_sel_hi:[0,1,0]
	v_fma_mix_f32 v72, v92, v145, v72 op_sel_hi:[0,1,0]
	v_fma_mix_f32 v73, v92, v145, v73 op_sel:[0,1,0] op_sel_hi:[0,1,0]
	v_fma_mix_f32 v74, v92, v146, v74 op_sel_hi:[0,1,0]
	v_fma_mix_f32 v75, v92, v146, v75 op_sel:[0,1,0] op_sel_hi:[0,1,0]
	v_fma_mix_f32 v76, v92, v147, v76 op_sel_hi:[0,1,0]
	v_fma_mix_f32 v77, v92, v147, v77 op_sel:[0,1,0] op_sel_hi:[0,1,0]
	ds_read_b128 v[180:183], v112 offset:20736
	ds_read_b128 v[184:187], v112 offset:21760
	ds_read_b128 v[188:191], v112 offset:22784
	ds_read_b128 v[108:111], v112 offset:23808
	s_waitcnt lgkmcnt(11)
	v_fma_mix_f32 v70, v93, v148, v70 op_sel_hi:[0,1,0]
	v_fma_mix_f32 v71, v93, v148, v71 op_sel:[0,1,0] op_sel_hi:[0,1,0]
	v_fma_mix_f32 v72, v93, v149, v72 op_sel_hi:[0,1,0]
	v_fma_mix_f32 v73, v93, v149, v73 op_sel:[0,1,0] op_sel_hi:[0,1,0]
	v_fma_mix_f32 v74, v93, v150, v74 op_sel_hi:[0,1,0]
	v_fma_mix_f32 v75, v93, v150, v75 op_sel:[0,1,0] op_sel_hi:[0,1,0]
	v_fma_mix_f32 v76, v93, v151, v76 op_sel_hi:[0,1,0]
	v_fma_mix_f32 v77, v93, v151, v77 op_sel:[0,1,0] op_sel_hi:[0,1,0]
	s_waitcnt lgkmcnt(10)
	v_fma_mix_f32 v70, v94, v152, v70 op_sel_hi:[0,1,0]
	v_fma_mix_f32 v71, v94, v152, v71 op_sel:[0,1,0] op_sel_hi:[0,1,0]
	v_fma_mix_f32 v72, v94, v153, v72 op_sel_hi:[0,1,0]
	v_fma_mix_f32 v73, v94, v153, v73 op_sel:[0,1,0] op_sel_hi:[0,1,0]
	v_fma_mix_f32 v74, v94, v154, v74 op_sel_hi:[0,1,0]
	v_fma_mix_f32 v75, v94, v154, v75 op_sel:[0,1,0] op_sel_hi:[0,1,0]
	v_fma_mix_f32 v76, v94, v155, v76 op_sel_hi:[0,1,0]
	v_fma_mix_f32 v77, v94, v155, v77 op_sel:[0,1,0] op_sel_hi:[0,1,0]
	s_waitcnt lgkmcnt(9)
	v_fma_mix_f32 v70, v95, v156, v70 op_sel_hi:[0,1,0]
	v_fma_mix_f32 v71, v95, v156, v71 op_sel:[0,1,0] op_sel_hi:[0,1,0]
	v_fma_mix_f32 v72, v95, v157, v72 op_sel_hi:[0,1,0]
	v_fma_mix_f32 v73, v95, v157, v73 op_sel:[0,1,0] op_sel_hi:[0,1,0]
	v_fma_mix_f32 v74, v95, v158, v74 op_sel_hi:[0,1,0]
	v_fma_mix_f32 v75, v95, v158, v75 op_sel:[0,1,0] op_sel_hi:[0,1,0]
	v_fma_mix_f32 v76, v95, v159, v76 op_sel_hi:[0,1,0]
	v_fma_mix_f32 v77, v95, v159, v77 op_sel:[0,1,0] op_sel_hi:[0,1,0]
	s_waitcnt lgkmcnt(8)
	v_fma_mix_f32 v70, v96, v160, v70 op_sel_hi:[0,1,0]
	v_fma_mix_f32 v71, v96, v160, v71 op_sel:[0,1,0] op_sel_hi:[0,1,0]
	v_fma_mix_f32 v72, v96, v161, v72 op_sel_hi:[0,1,0]
	v_fma_mix_f32 v73, v96, v161, v73 op_sel:[0,1,0] op_sel_hi:[0,1,0]
	v_fma_mix_f32 v74, v96, v162, v74 op_sel_hi:[0,1,0]
	v_fma_mix_f32 v75, v96, v162, v75 op_sel:[0,1,0] op_sel_hi:[0,1,0]
	v_fma_mix_f32 v76, v96, v163, v76 op_sel_hi:[0,1,0]
	v_fma_mix_f32 v77, v96, v163, v77 op_sel:[0,1,0] op_sel_hi:[0,1,0]
	s_waitcnt lgkmcnt(7)
	v_fma_mix_f32 v70, v98, v164, v70 op_sel_hi:[0,1,0]
	v_fma_mix_f32 v71, v98, v164, v71 op_sel:[0,1,0] op_sel_hi:[0,1,0]
	v_fma_mix_f32 v72, v98, v165, v72 op_sel_hi:[0,1,0]
	v_fma_mix_f32 v73, v98, v165, v73 op_sel:[0,1,0] op_sel_hi:[0,1,0]
	v_fma_mix_f32 v74, v98, v166, v74 op_sel_hi:[0,1,0]
	v_fma_mix_f32 v75, v98, v166, v75 op_sel:[0,1,0] op_sel_hi:[0,1,0]
	v_fma_mix_f32 v76, v98, v167, v76 op_sel_hi:[0,1,0]
	v_fma_mix_f32 v77, v98, v167, v77 op_sel:[0,1,0] op_sel_hi:[0,1,0]
	s_waitcnt lgkmcnt(6)
	v_fma_mix_f32 v70, v84, v168, v70 op_sel_hi:[0,1,0]
	v_fma_mix_f32 v71, v84, v168, v71 op_sel:[0,1,0] op_sel_hi:[0,1,0]
	v_fma_mix_f32 v72, v84, v169, v72 op_sel_hi:[0,1,0]
	v_fma_mix_f32 v73, v84, v169, v73 op_sel:[0,1,0] op_sel_hi:[0,1,0]
	v_fma_mix_f32 v74, v84, v170, v74 op_sel_hi:[0,1,0]
	v_fma_mix_f32 v75, v84, v170, v75 op_sel:[0,1,0] op_sel_hi:[0,1,0]
	v_fma_mix_f32 v76, v84, v171, v76 op_sel_hi:[0,1,0]
	v_fma_mix_f32 v77, v84, v171, v77 op_sel:[0,1,0] op_sel_hi:[0,1,0]
	s_waitcnt lgkmcnt(5)
	v_fma_mix_f32 v70, v99, v172, v70 op_sel_hi:[0,1,0]
	v_fma_mix_f32 v71, v99, v172, v71 op_sel:[0,1,0] op_sel_hi:[0,1,0]
	v_fma_mix_f32 v72, v99, v173, v72 op_sel_hi:[0,1,0]
	v_fma_mix_f32 v73, v99, v173, v73 op_sel:[0,1,0] op_sel_hi:[0,1,0]
	v_fma_mix_f32 v74, v99, v174, v74 op_sel_hi:[0,1,0]
	v_fma_mix_f32 v75, v99, v174, v75 op_sel:[0,1,0] op_sel_hi:[0,1,0]
	v_fma_mix_f32 v76, v99, v175, v76 op_sel_hi:[0,1,0]
	v_fma_mix_f32 v77, v99, v175, v77 op_sel:[0,1,0] op_sel_hi:[0,1,0]
	s_waitcnt lgkmcnt(4)
	v_fma_mix_f32 v70, v85, v176, v70 op_sel_hi:[0,1,0]
	v_fma_mix_f32 v71, v85, v176, v71 op_sel:[0,1,0] op_sel_hi:[0,1,0]
	v_fma_mix_f32 v72, v85, v177, v72 op_sel_hi:[0,1,0]
	v_fma_mix_f32 v73, v85, v177, v73 op_sel:[0,1,0] op_sel_hi:[0,1,0]
	v_fma_mix_f32 v74, v85, v178, v74 op_sel_hi:[0,1,0]
	v_fma_mix_f32 v75, v85, v178, v75 op_sel:[0,1,0] op_sel_hi:[0,1,0]
	v_fma_mix_f32 v76, v85, v179, v76 op_sel_hi:[0,1,0]
	v_fma_mix_f32 v77, v85, v179, v77 op_sel:[0,1,0] op_sel_hi:[0,1,0]
	s_waitcnt lgkmcnt(3)
	v_fma_mix_f32 v70, v27, v180, v70 op_sel_hi:[0,1,0]
	v_fma_mix_f32 v71, v27, v180, v71 op_sel:[0,1,0] op_sel_hi:[0,1,0]
	v_fma_mix_f32 v72, v27, v181, v72 op_sel_hi:[0,1,0]
	v_fma_mix_f32 v73, v27, v181, v73 op_sel:[0,1,0] op_sel_hi:[0,1,0]
	v_fma_mix_f32 v74, v27, v182, v74 op_sel_hi:[0,1,0]
	v_fma_mix_f32 v75, v27, v182, v75 op_sel:[0,1,0] op_sel_hi:[0,1,0]
	v_fma_mix_f32 v76, v27, v183, v76 op_sel_hi:[0,1,0]
	v_fma_mix_f32 v77, v27, v183, v77 op_sel:[0,1,0] op_sel_hi:[0,1,0]
	s_waitcnt lgkmcnt(2)
; template <int CTRL, int ROWMASK> __device__ __forceinline__ float dppf_(float x) { return __builtin_bit_cast(float, __builtin_amdgcn_update_dpp(0, __builtin_bit_cast(int, x), CTRL, ROWMASK, 0xf, false)); }
; __device__ __forceinline__ float wave_sum(float v) {
;     v += dppf_<0xB1, 0xf>(v); v += dppf_<0x4E, 0xf>(v); v += dppf_<0x141, 0xf>(v); v += dppf_<0x140, 0xf>(v);
;     v += dppf_<0x142, 0xa>(v);
;     v += dppf_<0x143, 0xc>(v);
;     return __builtin_bit_cast(float, __builtin_amdgcn_readlane(__builtin_bit_cast(int, v), 63));
; }
; __device__ __forceinline__ void router_ph(const int WID_, const bf16* __restrict__ x3, const float* __restrict__ nw, const float* __restrict__ wrg, const float* __restrict__ brg, ...
;     ...
; #pragma unroll
;         for (int i = 0; i < 8; ++i) l2[i] = wave_sum(l2[i]) + bre_l[grp * 8 + i];
	v_fma_mix_f32 v70, v26, v184, v70 op_sel_hi:[0,1,0]
	v_fma_mix_f32 v71, v26, v184, v71 op_sel:[0,1,0] op_sel_hi:[0,1,0]
	v_fma_mix_f32 v72, v26, v185, v72 op_sel_hi:[0,1,0]
	v_fma_mix_f32 v73, v26, v185, v73 op_sel:[0,1,0] op_sel_hi:[0,1,0]
	v_fma_mix_f32 v74, v26, v186, v74 op_sel_hi:[0,1,0]
	v_fma_mix_f32 v75, v26, v186, v75 op_sel:[0,1,0] op_sel_hi:[0,1,0]
	v_fma_mix_f32 v76, v26, v187, v76 op_sel_hi:[0,1,0]
	v_fma_mix_f32 v77, v26, v187, v77 op_sel:[0,1,0] op_sel_hi:[0,1,0]
	s_waitcnt lgkmcnt(1)
	v_fma_mix_f32 v70, v25, v188, v70 op_sel_hi:[0,1,0]
	v_fma_mix_f32 v71, v25, v188, v71 op_sel:[0,1,0] op_sel_hi:[0,1,0]
	v_fma_mix_f32 v72, v25, v189, v72 op_sel_hi:[0,1,0]
	v_fma_mix_f32 v73, v25, v189, v73 op_sel:[0,1,0] op_sel_hi:[0,1,0]
	v_fma_mix_f32 v74, v25, v190, v74 op_sel_hi:[0,1,0]
	v_fma_mix_f32 v75, v25, v190, v75 op_sel:[0,1,0] op_sel_hi:[0,1,0]
	v_fma_mix_f32 v76, v25, v191, v76 op_sel_hi:[0,1,0]
	v_fma_mix_f32 v77, v25, v191, v77 op_sel:[0,1,0] op_sel_hi:[0,1,0]
	s_waitcnt lgkmcnt(0)
	v_fma_mix_f32 v70, v24, v108, v70 op_sel_hi:[0,1,0]
	v_fma_mix_f32 v71, v24, v108, v71 op_sel:[0,1,0] op_sel_hi:[0,1,0]
	v_fma_mix_f32 v72, v24, v109, v72 op_sel_hi:[0,1,0]
	v_fma_mix_f32 v73, v24, v109, v73 op_sel:[0,1,0] op_sel_hi:[0,1,0]
	v_fma_mix_f32 v74, v24, v110, v74 op_sel_hi:[0,1,0]
	v_fma_mix_f32 v75, v24, v110, v75 op_sel:[0,1,0] op_sel_hi:[0,1,0]
	v_fma_mix_f32 v76, v24, v111, v76 op_sel_hi:[0,1,0]
	v_fma_mix_f32 v77, v24, v111, v77 op_sel:[0,1,0] op_sel_hi:[0,1,0]
	v_mov_b32_e32 v26, v70
	v_mov_b32_e32 v27, v71
	v_mov_b32_e32 v62, v72
	v_mov_b32_e32 v63, v73
	v_mov_b32_e32 v65, v74
	v_mov_b32_e32 v64, v75
	v_mov_b32_e32 v66, v76
	v_mov_b32_e32 v24, v77
	v_add_f32_dpp v26, v26, v26 quad_perm:[1,0,3,2] row_mask:0xf bank_mask:0xf bound_ctrl:1
	v_add_f32_dpp v27, v27, v27 quad_perm:[1,0,3,2] row_mask:0xf bank_mask:0xf bound_ctrl:1
	v_add_f32_dpp v62, v62, v62 quad_perm:[1,0,3,2] row_mask:0xf bank_mask:0xf bound_ctrl:1
	v_add_f32_dpp v63, v63, v63 quad_perm:[1,0,3,2] row_mask:0xf bank_mask:0xf bound_ctrl:1
	v_add_f32_dpp v65, v65, v65 quad_perm:[1,0,3,2] row_mask:0xf bank_mask:0xf bound_ctrl:1
	v_add_f32_dpp v64, v64, v64 quad_perm:[1,0,3,2] row_mask:0xf bank_mask:0xf bound_ctrl:1
	v_add_f32_dpp v66, v66, v66 quad_perm:[1,0,3,2] row_mask:0xf bank_mask:0xf bound_ctrl:1
	v_add_f32_dpp v24, v24, v24 quad_perm:[1,0,3,2] row_mask:0xf bank_mask:0xf bound_ctrl:1
	v_add_f32_dpp v26, v26, v26 quad_perm:[2,3,0,1] row_mask:0xf bank_mask:0xf bound_ctrl:1
	v_add_f32_dpp v27, v27, v27 quad_perm:[2,3,0,1] row_mask:0xf bank_mask:0xf bound_ctrl:1
	v_add_f32_dpp v62, v62, v62 quad_perm:[2,3,0,1] row_mask:0xf bank_mask:0xf bound_ctrl:1
	v_add_f32_dpp v63, v63, v63 quad_perm:[2,3,0,1] row_mask:0xf bank_mask:0xf bound_ctrl:1
	v_add_f32_dpp v65, v65, v65 quad_perm:[2,3,0,1] row_mask:0xf bank_mask:0xf bound_ctrl:1
	v_add_f32_dpp v64, v64, v64 quad_perm:[2,3,0,1] row_mask:0xf bank_mask:0xf bound_ctrl:1
	v_add_f32_dpp v66, v66, v66 quad_perm:[2,3,0,1] row_mask:0xf bank_mask:0xf bound_ctrl:1
	v_add_f32_dpp v24, v24, v24 quad_perm:[2,3,0,1] row_mask:0xf bank_mask:0xf bound_ctrl:1
	v_add_f32_dpp v26, v26, v26 row_half_mirror row_mask:0xf bank_mask:0xf bound_ctrl:1
	v_add_f32_dpp v27, v27, v27 row_half_mirror row_mask:0xf bank_mask:0xf bound_ctrl:1
	v_add_f32_dpp v62, v62, v62 row_half_mirror row_mask:0xf bank_mask:0xf bound_ctrl:1
	v_add_f32_dpp v63, v63, v63 row_half_mirror row_mask:0xf bank_mask:0xf bound_ctrl:1
	v_add_f32_dpp v65, v65, v65 row_half_mirror row_mask:0xf bank_mask:0xf bound_ctrl:1
	v_add_f32_dpp v64, v64, v64 row_half_mirror row_mask:0xf bank_mask:0xf bound_ctrl:1
	v_add_f32_dpp v66, v66, v66 row_half_mirror row_mask:0xf bank_mask:0xf bound_ctrl:1
	v_add_f32_dpp v24, v24, v24 row_half_mirror row_mask:0xf bank_mask:0xf bound_ctrl:1
	v_add_f32_dpp v26, v26, v26 row_mirror row_mask:0xf bank_mask:0xf bound_ctrl:1
	v_add_f32_dpp v27, v27, v27 row_mirror row_mask:0xf bank_mask:0xf bound_ctrl:1
	v_add_f32_dpp v62, v62, v62 row_mirror row_mask:0xf bank_mask:0xf bound_ctrl:1
	v_add_f32_dpp v63, v63, v63 row_mirror row_mask:0xf bank_mask:0xf bound_ctrl:1
	v_add_f32_dpp v65, v65, v65 row_mirror row_mask:0xf bank_mask:0xf bound_ctrl:1
	v_add_f32_dpp v64, v64, v64 row_mirror row_mask:0xf bank_mask:0xf bound_ctrl:1
	v_add_f32_dpp v66, v66, v66 row_mirror row_mask:0xf bank_mask:0xf bound_ctrl:1
	v_add_f32_dpp v24, v24, v24 row_mirror row_mask:0xf bank_mask:0xf bound_ctrl:1
	v_mov_b32_e32 v100, 0
	v_mov_b32_e32 v101, 0
	v_mov_b32_e32 v102, 0
	v_mov_b32_e32 v103, 0
	v_mov_b32_e32 v104, 0
	v_mov_b32_e32 v105, 0
	v_mov_b32_e32 v106, 0
	v_mov_b32_e32 v107, 0
	v_mov_b32_dpp v100, v26 row_bcast:15 row_mask:0xa bank_mask:0xf
	v_mov_b32_dpp v101, v27 row_bcast:15 row_mask:0xa bank_mask:0xf
	v_mov_b32_dpp v102, v62 row_bcast:15 row_mask:0xa bank_mask:0xf
	v_mov_b32_dpp v103, v63 row_bcast:15 row_mask:0xa bank_mask:0xf
	v_mov_b32_dpp v104, v65 row_bcast:15 row_mask:0xa bank_mask:0xf
	v_mov_b32_dpp v105, v64 row_bcast:15 row_mask:0xa bank_mask:0xf
	v_mov_b32_dpp v106, v66 row_bcast:15 row_mask:0xa bank_mask:0xf
	v_mov_b32_dpp v107, v24 row_bcast:15 row_mask:0xa bank_mask:0xf
	v_add_f32_e32 v26, v26, v100
	v_add_f32_e32 v27, v27, v101
	v_add_f32_e32 v62, v62, v102
	v_add_f32_e32 v63, v63, v103
	v_add_f32_e32 v65, v65, v104
	v_add_f32_e32 v64, v64, v105
	v_add_f32_e32 v66, v66, v106
	v_add_f32_e32 v24, v24, v107
	v_mov_b32_e32 v100, 0
	v_mov_b32_e32 v101, 0
	v_mov_b32_e32 v102, 0
	v_mov_b32_e32 v103, 0
	v_mov_b32_e32 v104, 0
	v_mov_b32_e32 v105, 0
	v_mov_b32_e32 v106, 0
	v_mov_b32_e32 v107, 0
	v_mov_b32_dpp v100, v26 row_bcast:31 row_mask:0xc bank_mask:0xf
	v_mov_b32_dpp v101, v27 row_bcast:31 row_mask:0xc bank_mask:0xf
	v_mov_b32_dpp v102, v62 row_bcast:31 row_mask:0xc bank_mask:0xf
	v_mov_b32_dpp v103, v63 row_bcast:31 row_mask:0xc bank_mask:0xf
	v_mov_b32_dpp v104, v65 row_bcast:31 row_mask:0xc bank_mask:0xf
	v_mov_b32_dpp v105, v64 row_bcast:31 row_mask:0xc bank_mask:0xf
	v_mov_b32_dpp v106, v66 row_bcast:31 row_mask:0xc bank_mask:0xf
	v_mov_b32_dpp v107, v24 row_bcast:31 row_mask:0xc bank_mask:0xf
	v_add_f32_e32 v26, v26, v100
	v_add_f32_e32 v27, v27, v101
	v_add_f32_e32 v62, v62, v102
	v_add_f32_e32 v63, v63, v103
	v_add_f32_e32 v65, v65, v104
	v_add_f32_e32 v64, v64, v105
	v_add_f32_e32 v66, v66, v106
	v_add_f32_e32 v24, v24, v107
	v_readlane_b32 s4, v26, 63
	v_readlane_b32 s5, v27, 63
	v_readlane_b32 s6, v62, 63
	v_readlane_b32 s7, v63, 63
	v_readlane_b32 s8, v65, 63
	v_readlane_b32 s9, v64, 63
	v_readlane_b32 s10, v66, 63
	v_readlane_b32 s11, v24, 63
	s_lshl_b64 s[100:101], 1, s99
	s_add_i32 s99, s99, 1
	s_mov_b64 exec, s[100:101]
	v_mov_b32_e32 v200, v22
	v_mov_b32_e32 v201, v23
	v_mov_b32_e32 v202, v59
	v_mov_b32_e32 v203, v60
	v_mov_b32_e32 v204, s4
	v_mov_b32_e32 v205, s5
	v_mov_b32_e32 v206, s6
	v_mov_b32_e32 v207, s7
	v_mov_b32_e32 v208, s8
	v_mov_b32_e32 v209, s9
	v_mov_b32_e32 v210, s10
	v_mov_b32_e32 v211, s11
	v_mov_b32_e32 v212, v2
	v_mov_b32_e32 v213, s49
	s_mov_b64 exec, -1
	s_waitcnt vmcnt(0)

; __device__ __forceinline__ void router_ph(const int WID_, const bf16* __restrict__ x3, const float* __restrict__ nw, const float* __restrict__ wrg, const float* __restrict__ brg, ...
;     ...
;         for (int i = 0; i < 4; ++i) l1[i] = wave_sum(l1[i]) + brg_l[i];
;         int grp = 0; float best = l1[0];
; #pragma unroll
;         for (int i = 1; i < 4; ++i) if (l1[i] > best) { best = l1[i]; grp = i; }
;         float se = 0.f;
; #pragma unroll
;         for (int i = 0; i < 4; ++i) se += __expf(l1[i] - best);
;         const float g1 = 1.f / se;
;         float l2[8] = {};
;         const _Float16* we = we16 + (size_t)grp * D * 8;
; #pragma unroll
;         for (int j = 0; j < 2; ++j) {
;             const int k0 = (lane + 64 * j) * 8;
; #pragma unroll
;             for (int e = 0; e < 8; ++e) { const float x = h[8 * j + e]; const h8 w = *(const h8*)(we + (k0 + e) * 8);
; #pragma unroll
;                 for (int q = 0; q < 8; ++q) l2[q] += x * (float)w[q]; }
;         }
; #pragma unroll
;         for (int i = 0; i < 8; ++i) l2[i] = wave_sum(l2[i]) + bre_l[grp * 8 + i];
;         int i0 = 0; float v0 = l2[0];
; #pragma unroll
;         for (int i = 1; i < 8; ++i) if (l2[i] > v0) { v0 = l2[i]; i0 = i; }
;         int i1 = -1; float v1 = -3.0e38f;
; #pragma unroll
;         for (int i = 0; i < 8; ++i) if (i != i0 && l2[i] > v1) { v1 = l2[i]; i1 = i; }
;         const float e1 = __expf(v1 - v0), inv = 1.f / (1.f + e1);
;         if (lane == 0) {
;             const int ea = grp * 8 + i0, eb = grp * 8 + i1;
;             mb.tok_e[2 * m] = ea; mb.tok_e[2 * m + 1] = eb; mb.tok_rs[m] = rs;
;             mb.tok_g[2 * m] = g1 * inv; mb.tok_g[2 * m + 1] = g1 * e1 * inv;
;             atomicAdd(&lcnt[ea], 1); atomicAdd(&lcnt[eb], 1);
;         }
;     }
;     __syncthreads();
;     if (wv == 0 && lane < 32) mb.bcnt[tile * 32 + lane] = lcnt[lane];
.LBB0_2150:
	s_mov_b32 exec_lo, -1
	s_mov_b32 exec_hi, 0
	v_lshlrev_b32_e32 v226, 5, v213
	ds_read_b128 v[220:223], v226 offset:128
	ds_read_b128 v[224:227], v226 offset:144
	s_waitcnt lgkmcnt(0)
	v_add_f32_e32 v204, v204, v220
	v_add_f32_e32 v205, v205, v221
	v_add_f32_e32 v206, v206, v222
	v_add_f32_e32 v207, v207, v223
	v_add_f32_e32 v208, v208, v224
	v_add_f32_e32 v209, v209, v225
	v_add_f32_e32 v210, v210, v226
	v_add_f32_e32 v211, v211, v227
	v_cmp_gt_f32_e32 vcc, v201, v200
	s_nop 1
	v_cndmask_b32_e32 v214, v200, v201, vcc
	v_cmp_gt_f32_e32 vcc, v202, v214
	s_nop 1
	v_cndmask_b32_e32 v214, v214, v202, vcc
	v_cmp_gt_f32_e32 vcc, v203, v214
	s_nop 1
	v_cndmask_b32_e32 v214, v214, v203, vcc
	v_sub_f32_e32 v215, v200, v214
	v_mul_f32_e32 v215, 0x3fb8aa3b, v215
	v_exp_f32_e32 v215, v215
	v_sub_f32_e32 v216, v201, v214
	v_mul_f32_e32 v216, 0x3fb8aa3b, v216
	v_exp_f32_e32 v216, v216
	v_sub_f32_e32 v217, v202, v214
	v_mul_f32_e32 v217, 0x3fb8aa3b, v217
	v_exp_f32_e32 v217, v217
	v_sub_f32_e32 v218, v203, v214
	v_mul_f32_e32 v218, 0x3fb8aa3b, v218
	v_exp_f32_e32 v218, v218
	s_nop 0
	v_add_f32_e32 v215, 0, v215
	v_add_f32_e32 v215, v216, v215
	v_add_f32_e32 v215, v217, v215
	v_add_f32_e32 v215, v218, v215
	v_div_scale_f32 v226, s[4:5], v215, v215, 1.0
	v_rcp_f32_e32 v227, v226
	v_div_scale_f32 v228, vcc, 1.0, v215, 1.0
	v_fma_f32 v229, -v226, v227, 1.0
	v_fmac_f32_e32 v227, v229, v227
	v_mul_f32_e32 v229, v228, v227
	v_fma_f32 v230, -v226, v229, v228
	v_fmac_f32_e32 v229, v230, v227
	v_fma_f32 v226, -v226, v229, v228
	v_div_fmas_f32 v226, v226, v227, v229
	v_div_fixup_f32 v215, v226, v215, 1.0
	v_mov_b32_e32 v216, v204
	v_mov_b32_e32 v217, 0
	v_cmp_gt_f32_e32 vcc, v205, v216
	s_nop 1
	v_cndmask_b32_e32 v216, v216, v205, vcc
	v_cndmask_b32_e64 v217, v217, 1, vcc
	v_cmp_gt_f32_e32 vcc, v206, v216
	s_nop 1
	v_cndmask_b32_e32 v216, v216, v206, vcc
	v_cndmask_b32_e64 v217, v217, 2, vcc
	v_cmp_gt_f32_e32 vcc, v207, v216
	s_nop 1
	v_cndmask_b32_e32 v216, v216, v207, vcc
	v_cndmask_b32_e64 v217, v217, 3, vcc
	v_cmp_gt_f32_e32 vcc, v208, v216
	s_nop 1
	v_cndmask_b32_e32 v216, v216, v208, vcc
	v_cndmask_b32_e64 v217, v217, 4, vcc
	v_cmp_gt_f32_e32 vcc, v209, v216
	s_nop 1
	v_cndmask_b32_e32 v216, v216, v209, vcc
	v_cndmask_b32_e64 v217, v217, 5, vcc
	v_cmp_gt_f32_e32 vcc, v210, v216
	s_nop 1
	v_cndmask_b32_e32 v216, v216, v210, vcc
	v_cndmask_b32_e64 v217, v217, 6, vcc
	v_cmp_gt_f32_e32 vcc, v211, v216
	s_nop 1
	v_cndmask_b32_e32 v216, v216, v211, vcc
	v_cndmask_b32_e64 v217, v217, 7, vcc
	v_mov_b32_e32 v218, 0xff61b1e6
	v_mov_b32_e32 v219, -1
	v_cmp_ne_u32_e64 s[4:5], 0, v217
	v_cmp_gt_f32_e64 s[6:7], v204, v218
	s_nop 1
	s_and_b64 vcc, s[4:5], s[6:7]
	v_cndmask_b32_e32 v218, v218, v204, vcc
	v_cndmask_b32_e64 v219, v219, 0, vcc
	v_cmp_ne_u32_e64 s[4:5], 1, v217
	v_cmp_gt_f32_e64 s[6:7], v205, v218
	s_nop 1
	s_and_b64 vcc, s[4:5], s[6:7]
	v_cndmask_b32_e32 v218, v218, v205, vcc
	v_cndmask_b32_e64 v219, v219, 1, vcc
	v_cmp_ne_u32_e64 s[4:5], 2, v217
	v_cmp_gt_f32_e64 s[6:7], v206, v218
	s_nop 1
	s_and_b64 vcc, s[4:5], s[6:7]
	v_cndmask_b32_e32 v218, v218, v206, vcc
	v_cndmask_b32_e64 v219, v219, 2, vcc
	v_cmp_ne_u32_e64 s[4:5], 3, v217
	v_cmp_gt_f32_e64 s[6:7], v207, v218
	s_nop 1
	s_and_b64 vcc, s[4:5], s[6:7]
	v_cndmask_b32_e32 v218, v218, v207, vcc
	v_cndmask_b32_e64 v219, v219, 3, vcc
	v_cmp_ne_u32_e64 s[4:5], 4, v217
	v_cmp_gt_f32_e64 s[6:7], v208, v218
	s_nop 1
	s_and_b64 vcc, s[4:5], s[6:7]
	v_cndmask_b32_e32 v218, v218, v208, vcc
	v_cndmask_b32_e64 v219, v219, 4, vcc
	v_cmp_ne_u32_e64 s[4:5], 5, v217
	v_cmp_gt_f32_e64 s[6:7], v209, v218
	s_nop 1
	s_and_b64 vcc, s[4:5], s[6:7]
	v_cndmask_b32_e32 v218, v218, v209, vcc
	v_cndmask_b32_e64 v219, v219, 5, vcc
	v_cmp_ne_u32_e64 s[4:5], 6, v217
	v_cmp_gt_f32_e64 s[6:7], v210, v218
	s_nop 1
	s_and_b64 vcc, s[4:5], s[6:7]
	v_cndmask_b32_e32 v218, v218, v210, vcc
	v_cndmask_b32_e64 v219, v219, 6, vcc
	v_cmp_ne_u32_e64 s[4:5], 7, v217
	v_cmp_gt_f32_e64 s[6:7], v211, v218
	s_nop 1
	s_and_b64 vcc, s[4:5], s[6:7]
	v_cndmask_b32_e32 v218, v218, v211, vcc
	v_cndmask_b32_e64 v219, v219, 7, vcc
	v_sub_f32_e32 v220, v218, v216
	v_mul_f32_e32 v220, 0x3fb8aa3b, v220
	v_exp_f32_e32 v220, v220
	s_nop 0
	v_add_f32_e32 v221, 1.0, v220
	v_div_scale_f32 v226, s[4:5], v221, v221, 1.0
	v_rcp_f32_e32 v227, v226
	v_div_scale_f32 v228, vcc, 1.0, v221, 1.0
	v_fma_f32 v229, -v226, v227, 1.0
	v_fmac_f32_e32 v227, v229, v227
	v_mul_f32_e32 v229, v228, v227
	v_fma_f32 v230, -v226, v229, v228
	v_fmac_f32_e32 v229, v230, v227
	v_fma_f32 v226, -v226, v229, v228
	v_div_fmas_f32 v226, v226, v227, v229
	v_div_fixup_f32 v221, v226, v221, 1.0
	v_lshl_add_u32 v222, v213, 3, v217
	v_lshl_add_u32 v223, v213, 3, v219
	v_mul_f32_e32 v224, v215, v221
	v_mul_f32_e32 v225, v215, v220
	v_mul_f32_e32 v225, v225, v221
	v_mbcnt_lo_u32_b32 v226, -1, 0
	v_mbcnt_hi_u32_b32 v226, -1, v226
	s_sub_i32 s4, s80, 0x200
	s_lshl_b32 s4, s4, 2
	v_lshl_add_u32 v227, v226, 6, s4
	s_add_u32 s6, s78, 0xfffffc00
	s_addc_u32 s7, s79, -1
	v_lshlrev_b32_e32 v228, 5, v226
	global_store_dwordx2 v227, v[222:223], s[52:53]
	global_store_dwordx2 v227, v[224:225], s[40:41]
	global_store_dword v228, v212, s[6:7]
	v_lshlrev_b32_e32 v229, 2, v222
	v_lshlrev_b32_e32 v230, 2, v223
	v_mov_b32_e32 v231, 1
	ds_add_u32 v229, v231
	ds_add_u32 v230, v231
	s_mov_b64 exec, -1
	s_waitcnt lgkmcnt(0)
	s_barrier
	s_and_saveexec_b64 s[2:3], s[24:25]
	s_cbranch_execz .LBB0_2006
	ds_read_b32 v2, v28
	v_lshl_add_u32 v0, s42, 5, v20
	v_readlane_b32 s0, v242, 41
	v_ashrrev_i32_e32 v1, 31, v0
	v_readlane_b32 s1, v242, 42
	s_nop 1
	v_lshl_add_u64 v[0:1], v[0:1], 2, s[0:1]
	s_waitcnt lgkmcnt(0)
	global_store_dword v[0:1], v2, off
	s_branch .LBB0_2006
